# v25 + no workgroup stagger delay before the MoE down GEMM
# baseline (speedup 1.0000x reference)
; __global__ void __launch_bounds__(NWAVES * 64, 2) mk_fwd(Args args) {
;     ...
;         if (IN(14) && STAG2 > 0) {
;             const unsigned long long t0 = __builtin_amdgcn_s_memrealtime(); const unsigned long long dl = (unsigned long long)(((F.bid >> 3) & 3) * STAG2);
;             while (__builtin_amdgcn_s_memrealtime() - t0 < dl) __builtin_amdgcn_s_sleep(8);
;         }
.LBB0_1683:
	s_cmp_lt_i32 s28, 15
	s_cselect_b64 s[6:7], -1, 0
	s_and_b64 s[4:5], s[6:7], s[4:5]
	s_andn2_b64 vcc, exec, s[4:5]
	s_cbranch_vccnz .LBB0_1708
	s_memrealtime s[4:5]
	s_memrealtime s[10:11]
	s_bfe_u32 s6, s2, 0x20003
	s_mov_b32 s7, 0
	s_mulk_i32 s6, 0x0
	v_mov_b64_e32 v[2:3], s[6:7]
	s_waitcnt lgkmcnt(0)
	s_sub_u32 s10, s10, s4
	s_subb_u32 s11, s11, s5
	v_cmp_ge_u64_e32 vcc, s[10:11], v[2:3]
	s_cbranch_vccnz .LBB0_1687
	v_mov_b64_e32 v[2:3], s[6:7]
